# grid barrier: first-barrier-only census block (3 KB) moved out of the arrival path (behind the branch entering the non-leader spin), arrival path now straight-line
# baseline (speedup 1.0000x reference)
.Lcwarm_0:
	s_mov_b64 s[0:1], exec
	v_readlane_b32 s4, v253, 15
	v_readlane_b32 s5, v253, 16
	s_and_b64 s[4:5], s[0:1], s[4:5]
	s_mov_b64 exec, s[4:5]
	s_cbranch_execz .LBB0_112
	s_add_i32 s4, 0, 0x27fc0
	v_mov_b32_e32 v0, s4
	s_waitcnt vmcnt(0) expcnt(0) lgkmcnt(0)
	ds_read_b32 v2, v0
	s_add_i32 s4, 0, 0x27fc4
	v_mov_b32_e32 v0, s4
	ds_read_b32 v0, v0
	s_waitcnt lgkmcnt(1)
	v_cmp_ne_u32_e32 vcc, 0, v2
	s_cbranch_vccz .Lcensus_0

.Lcensus_0:
	v_readlane_b32 s4, v253, 10
	v_readlane_b32 s5, v253, 11
	v_readlane_b32 s6, v253, 8
	s_mul_i32 s31, s5, s6
	s_mul_i32 s31, s31, s4
	s_add_u32 s4, s88, 0x80200
	s_addc_u32 s5, s89, 0
	s_add_u32 s6, s88, 0x80400
	s_addc_u32 s7, s89, 0
	s_add_u32 s8, s88, 0x80500
	s_addc_u32 s9, s89, 0
	s_add_u32 s10, s88, 0x80600
	s_addc_u32 s11, s89, 0
	s_add_u32 s12, s88, 0x80700
	s_addc_u32 s13, s89, 0
	s_add_u32 s14, s88, 0x80800
	s_addc_u32 s15, s89, 0
	s_add_u32 s16, s88, 0x80900
	s_addc_u32 s17, s89, 0
	s_add_u32 s18, s88, 0x80a00
	s_addc_u32 s19, s89, 0
	s_add_u32 s20, s88, 0x80b00
	s_addc_u32 s21, s89, 0
	s_add_u32 s22, s88, 0x80c00
	s_addc_u32 s23, s89, 0
	s_add_u32 s24, s88, 0x80d00
	s_addc_u32 s25, s89, 0
	s_add_u32 s26, s88, 0x80e00
	s_addc_u32 s27, s89, 0
	s_add_u32 s28, s88, 0x80f00
	s_addc_u32 s29, s89, 0
	s_add_u32 s34, s88, 0x81000
	s_addc_u32 s35, s89, 0
	s_add_u32 s40, s88, 0x81100
	s_addc_u32 s41, s89, 0
	s_add_u32 s44, s88, 0x81200
	s_addc_u32 s45, s89, 0
	s_add_u32 s52, s88, 0x81300
	s_addc_u32 s53, s89, 0
	s_mov_b32 s33, 1
	v_mov_b32_e32 v16, 0
	s_branch .LBB0_64

.LBB0_75:
	v_readlane_b32 s4, v253, 14
	s_cmp_eq_u32 s4, 0
	s_cselect_b64 vcc, -1, 0
	s_cmp_eq_u32 s4, 1
	v_cndmask_b32_e32 v16, 0, v15, vcc
	s_cselect_b64 vcc, -1, 0
	s_cmp_eq_u32 s4, 2
	v_cndmask_b32_e32 v16, v16, v0, vcc
	s_cselect_b64 vcc, -1, 0
	s_cmp_eq_u32 s4, 3
	v_cndmask_b32_e32 v16, v16, v1, vcc
	s_cselect_b64 vcc, -1, 0
	s_cmp_eq_u32 s4, 4
	v_cndmask_b32_e32 v16, v16, v2, vcc
	s_cselect_b64 vcc, -1, 0
	s_cmp_eq_u32 s4, 5
	v_cndmask_b32_e32 v16, v16, v3, vcc
	s_cselect_b64 vcc, -1, 0
	s_cmp_eq_u32 s4, 6
	v_cndmask_b32_e32 v16, v16, v4, vcc
	s_cselect_b64 vcc, -1, 0
	s_cmp_eq_u32 s4, 7
	v_cndmask_b32_e32 v16, v16, v5, vcc
	s_cselect_b64 vcc, -1, 0
	s_cmp_eq_u32 s4, 8
	v_cndmask_b32_e32 v16, v16, v6, vcc
	s_cselect_b64 vcc, -1, 0
	s_cmp_eq_u32 s4, 9
	v_cndmask_b32_e32 v16, v16, v7, vcc
	s_cselect_b64 vcc, -1, 0
	s_cmp_eq_u32 s4, 10
	v_cndmask_b32_e32 v16, v16, v8, vcc
	s_cselect_b64 vcc, -1, 0
	s_cmp_eq_u32 s4, 11
	v_cndmask_b32_e32 v16, v16, v9, vcc
	s_cselect_b64 vcc, -1, 0
	s_cmp_eq_u32 s4, 12
	v_cndmask_b32_e32 v16, v16, v10, vcc
	s_cselect_b64 vcc, -1, 0
	s_cmp_eq_u32 s4, 13
	v_cndmask_b32_e32 v16, v16, v11, vcc
	s_cselect_b64 vcc, -1, 0
	s_cmp_eq_u32 s4, 14
	v_cndmask_b32_e32 v16, v16, v12, vcc
	s_cselect_b64 vcc, -1, 0
	s_cmp_eq_u32 s4, 15
	v_cndmask_b32_e32 v16, v16, v13, vcc
	s_cselect_b64 vcc, -1, 0
	v_cndmask_b32_e32 v16, v16, v14, vcc
	v_cmp_ne_u32_e32 vcc, 0, v15
	s_add_i32 s4, 0, 0x27fc0
	s_nop 0
	v_cndmask_b32_e64 v15, 0, 1, vcc
	v_cmp_ne_u32_e32 vcc, 0, v0
	s_nop 1
	v_addc_co_u32_e32 v0, vcc, 0, v15, vcc
	v_cmp_ne_u32_e32 vcc, 0, v1
	s_nop 1
	v_cndmask_b32_e64 v1, 0, 1, vcc
	v_cmp_ne_u32_e32 vcc, 0, v2
	v_max_u32_e32 v2, 1, v16
	s_nop 0
	v_addc_co_u32_e32 v0, vcc, v0, v1, vcc
	v_cmp_ne_u32_e32 vcc, 0, v3
	s_nop 1
	v_cndmask_b32_e64 v1, 0, 1, vcc
	v_cmp_ne_u32_e32 vcc, 0, v4
	s_nop 1
	v_addc_co_u32_e32 v0, vcc, v0, v1, vcc
	v_cmp_ne_u32_e32 vcc, 0, v5
	s_nop 1
	v_cndmask_b32_e64 v1, 0, 1, vcc
	v_cmp_ne_u32_e32 vcc, 0, v6
	s_nop 1
	v_addc_co_u32_e32 v0, vcc, v0, v1, vcc
	v_cmp_ne_u32_e32 vcc, 0, v7
	s_nop 1
	v_cndmask_b32_e64 v1, 0, 1, vcc
	v_cmp_ne_u32_e32 vcc, 0, v8
	s_nop 1
	v_addc_co_u32_e32 v0, vcc, v0, v1, vcc
	v_cmp_ne_u32_e32 vcc, 0, v9
	s_nop 1
	v_cndmask_b32_e64 v1, 0, 1, vcc
	v_cmp_ne_u32_e32 vcc, 0, v10
	s_nop 1
	v_addc_co_u32_e32 v0, vcc, v0, v1, vcc
	v_cmp_ne_u32_e32 vcc, 0, v11
	s_nop 1
	v_cndmask_b32_e64 v1, 0, 1, vcc
	v_cmp_ne_u32_e32 vcc, 0, v12
	s_nop 1
	v_addc_co_u32_e32 v0, vcc, v0, v1, vcc
	v_cmp_ne_u32_e32 vcc, 0, v13
	s_nop 1
	v_cndmask_b32_e64 v1, 0, 1, vcc
	v_cmp_ne_u32_e32 vcc, 0, v14
	s_nop 1
	v_addc_co_u32_e32 v0, vcc, v0, v1, vcc
	v_mov_b32_e32 v1, s4
	s_add_i32 s4, 0, 0x27fc4
	v_max_u32_e32 v0, 1, v0
	ds_write_b32 v1, v2
	v_mov_b32_e32 v1, s4
	ds_write_b32 v1, v0
	s_branch .LBB0_76

.Lcwarm_1:
	s_mov_b64 s[4:5], exec
	v_readlane_b32 s6, v253, 15
	v_readlane_b32 s7, v253, 16
	s_and_b64 s[6:7], s[4:5], s[6:7]
	s_mov_b64 exec, s[6:7]
	s_cbranch_execz .LBB0_183
	s_add_i32 s6, 0, 0x27fc0
	v_mov_b32_e32 v0, s6
	s_waitcnt vmcnt(0) expcnt(0) lgkmcnt(0)
	ds_read_b32 v2, v0
	s_add_i32 s6, 0, 0x27fc4
	v_mov_b32_e32 v0, s6
	ds_read_b32 v0, v0
	s_waitcnt lgkmcnt(1)
	v_cmp_ne_u32_e32 vcc, 0, v2
	s_cbranch_vccz .Lcensus_1

.Lcensus_1:
	v_readlane_b32 s6, v253, 10
	v_readlane_b32 s7, v253, 11
	v_readlane_b32 s8, v253, 8
	s_mul_i32 s31, s7, s8
	s_mul_i32 s31, s31, s6
	s_add_u32 s6, s88, 0x80200
	s_addc_u32 s7, s89, 0
	s_add_u32 s8, s88, 0x80400
	s_addc_u32 s9, s89, 0
	s_add_u32 s10, s88, 0x80500
	s_addc_u32 s11, s89, 0
	s_add_u32 s12, s88, 0x80600
	s_addc_u32 s13, s89, 0
	s_add_u32 s14, s88, 0x80700
	s_addc_u32 s15, s89, 0
	s_add_u32 s16, s88, 0x80800
	s_addc_u32 s17, s89, 0
	s_add_u32 s18, s88, 0x80900
	s_addc_u32 s19, s89, 0
	s_add_u32 s20, s88, 0x80a00
	s_addc_u32 s21, s89, 0
	s_add_u32 s22, s88, 0x80b00
	s_addc_u32 s23, s89, 0
	s_add_u32 s24, s88, 0x80c00
	s_addc_u32 s25, s89, 0
	s_add_u32 s26, s88, 0x80d00
	s_addc_u32 s27, s89, 0
	s_add_u32 s28, s88, 0x80e00
	s_addc_u32 s29, s89, 0
	s_add_u32 s34, s88, 0x80f00
	s_addc_u32 s35, s89, 0
	s_add_u32 s40, s88, 0x81000
	s_addc_u32 s41, s89, 0
	s_add_u32 s44, s88, 0x81100
	s_addc_u32 s45, s89, 0
	s_add_u32 s52, s88, 0x81200
	s_addc_u32 s53, s89, 0
	s_add_u32 s68, s88, 0x81300
	s_addc_u32 s69, s89, 0
	s_mov_b32 s33, 1
	v_mov_b32_e32 v16, 0
	s_branch .LBB0_135

.LBB0_146:
	v_readlane_b32 s6, v253, 14
	s_cmp_eq_u32 s6, 0
	s_cselect_b64 vcc, -1, 0
	s_cmp_eq_u32 s6, 1
	v_cndmask_b32_e32 v16, 0, v15, vcc
	s_cselect_b64 vcc, -1, 0
	s_cmp_eq_u32 s6, 2
	v_cndmask_b32_e32 v16, v16, v0, vcc
	s_cselect_b64 vcc, -1, 0
	s_cmp_eq_u32 s6, 3
	v_cndmask_b32_e32 v16, v16, v1, vcc
	s_cselect_b64 vcc, -1, 0
	s_cmp_eq_u32 s6, 4
	v_cndmask_b32_e32 v16, v16, v2, vcc
	s_cselect_b64 vcc, -1, 0
	s_cmp_eq_u32 s6, 5
	v_cndmask_b32_e32 v16, v16, v3, vcc
	s_cselect_b64 vcc, -1, 0
	s_cmp_eq_u32 s6, 6
	v_cndmask_b32_e32 v16, v16, v4, vcc
	s_cselect_b64 vcc, -1, 0
	s_cmp_eq_u32 s6, 7
	v_cndmask_b32_e32 v16, v16, v5, vcc
	s_cselect_b64 vcc, -1, 0
	s_cmp_eq_u32 s6, 8
	v_cndmask_b32_e32 v16, v16, v6, vcc
	s_cselect_b64 vcc, -1, 0
	s_cmp_eq_u32 s6, 9
	v_cndmask_b32_e32 v16, v16, v7, vcc
	s_cselect_b64 vcc, -1, 0
	s_cmp_eq_u32 s6, 10
	v_cndmask_b32_e32 v16, v16, v8, vcc
	s_cselect_b64 vcc, -1, 0
	s_cmp_eq_u32 s6, 11
	v_cndmask_b32_e32 v16, v16, v9, vcc
	s_cselect_b64 vcc, -1, 0
	s_cmp_eq_u32 s6, 12
	v_cndmask_b32_e32 v16, v16, v10, vcc
	s_cselect_b64 vcc, -1, 0
	s_cmp_eq_u32 s6, 13
	v_cndmask_b32_e32 v16, v16, v11, vcc
	s_cselect_b64 vcc, -1, 0
	s_cmp_eq_u32 s6, 14
	v_cndmask_b32_e32 v16, v16, v12, vcc
	s_cselect_b64 vcc, -1, 0
	s_cmp_eq_u32 s6, 15
	v_cndmask_b32_e32 v16, v16, v13, vcc
	s_cselect_b64 vcc, -1, 0
	v_cndmask_b32_e32 v16, v16, v14, vcc
	v_cmp_ne_u32_e32 vcc, 0, v15
	s_add_i32 s6, 0, 0x27fc0
	s_nop 0
	v_cndmask_b32_e64 v15, 0, 1, vcc
	v_cmp_ne_u32_e32 vcc, 0, v0
	s_nop 1
	v_addc_co_u32_e32 v0, vcc, 0, v15, vcc
	v_cmp_ne_u32_e32 vcc, 0, v1
	s_nop 1
	v_cndmask_b32_e64 v1, 0, 1, vcc
	v_cmp_ne_u32_e32 vcc, 0, v2
	v_max_u32_e32 v2, 1, v16
	s_nop 0
	v_addc_co_u32_e32 v0, vcc, v0, v1, vcc
	v_cmp_ne_u32_e32 vcc, 0, v3
	s_nop 1
	v_cndmask_b32_e64 v1, 0, 1, vcc
	v_cmp_ne_u32_e32 vcc, 0, v4
	s_nop 1
	v_addc_co_u32_e32 v0, vcc, v0, v1, vcc
	v_cmp_ne_u32_e32 vcc, 0, v5
	s_nop 1
	v_cndmask_b32_e64 v1, 0, 1, vcc
	v_cmp_ne_u32_e32 vcc, 0, v6
	s_nop 1
	v_addc_co_u32_e32 v0, vcc, v0, v1, vcc
	v_cmp_ne_u32_e32 vcc, 0, v7
	s_nop 1
	v_cndmask_b32_e64 v1, 0, 1, vcc
	v_cmp_ne_u32_e32 vcc, 0, v8
	s_nop 1
	v_addc_co_u32_e32 v0, vcc, v0, v1, vcc
	v_cmp_ne_u32_e32 vcc, 0, v9
	s_nop 1
	v_cndmask_b32_e64 v1, 0, 1, vcc
	v_cmp_ne_u32_e32 vcc, 0, v10
	s_nop 1
	v_addc_co_u32_e32 v0, vcc, v0, v1, vcc
	v_cmp_ne_u32_e32 vcc, 0, v11
	s_nop 1
	v_cndmask_b32_e64 v1, 0, 1, vcc
	v_cmp_ne_u32_e32 vcc, 0, v12
	s_nop 1
	v_addc_co_u32_e32 v0, vcc, v0, v1, vcc
	v_cmp_ne_u32_e32 vcc, 0, v13
	s_nop 1
	v_cndmask_b32_e64 v1, 0, 1, vcc
	v_cmp_ne_u32_e32 vcc, 0, v14
	s_nop 1
	v_addc_co_u32_e32 v0, vcc, v0, v1, vcc
	v_mov_b32_e32 v1, s6
	s_add_i32 s6, 0, 0x27fc4
	v_max_u32_e32 v0, 1, v0
	ds_write_b32 v1, v2
	v_mov_b32_e32 v1, s6
	ds_write_b32 v1, v0
	s_branch .LBB0_147

.Lcwarm_2:
	s_mov_b64 s[2:3], exec
	v_readlane_b32 s4, v253, 15
	v_readlane_b32 s5, v253, 16
	s_and_b64 s[4:5], s[2:3], s[4:5]
	s_mov_b64 exec, s[4:5]
	s_cbranch_execz .LBB0_400
	s_add_i32 s4, 0, 0x27fc0
	v_mov_b32_e32 v0, s4
	s_waitcnt vmcnt(0) expcnt(0) lgkmcnt(0)
	ds_read_b32 v2, v0
	s_add_i32 s4, 0, 0x27fc4
	v_mov_b32_e32 v0, s4
	ds_read_b32 v0, v0
	s_waitcnt lgkmcnt(1)
	v_cmp_ne_u32_e32 vcc, 0, v2
	s_cbranch_vccz .Lcensus_2

.Lcensus_2:
	v_readlane_b32 s4, v253, 8
	s_mul_i32 s31, s77, s4
	s_add_u32 s4, s88, 0x80200
	s_addc_u32 s5, s89, 0
	s_add_u32 s6, s88, 0x80400
	s_addc_u32 s7, s89, 0
	s_add_u32 s8, s88, 0x80500
	s_addc_u32 s9, s89, 0
	s_add_u32 s10, s88, 0x80600
	s_addc_u32 s11, s89, 0
	s_add_u32 s12, s88, 0x80700
	s_addc_u32 s13, s89, 0
	s_add_u32 s14, s88, 0x80800
	s_addc_u32 s15, s89, 0
	s_add_u32 s16, s88, 0x80900
	s_addc_u32 s17, s89, 0
	s_add_u32 s18, s88, 0x80a00
	s_addc_u32 s19, s89, 0
	s_add_u32 s20, s88, 0x80b00
	s_addc_u32 s21, s89, 0
	s_add_u32 s22, s88, 0x80c00
	s_addc_u32 s23, s89, 0
	s_add_u32 s24, s88, 0x80d00
	s_addc_u32 s25, s89, 0
	s_add_u32 s26, s88, 0x80e00
	s_addc_u32 s27, s89, 0
	s_add_u32 s28, s88, 0x80f00
	s_addc_u32 s29, s89, 0
	s_add_u32 s34, s88, 0x81000
	s_addc_u32 s35, s89, 0
	s_add_u32 s52, s88, 0x81100
	s_addc_u32 s53, s89, 0
	s_add_u32 s54, s88, 0x81200
	s_addc_u32 s55, s89, 0
	s_add_u32 s56, s88, 0x81300
	s_mul_i32 s31, s31, s76
	s_addc_u32 s57, s89, 0
	s_mov_b32 s33, 1
	v_mov_b32_e32 v16, 0
	s_branch .LBB0_352

.Lcwarm_3:
	s_mov_b64 s[0:1], exec
	v_readlane_b32 s4, v253, 15
	v_readlane_b32 s5, v253, 16
	s_and_b64 s[4:5], s[0:1], s[4:5]
	s_mov_b64 exec, s[4:5]
	s_cbranch_execz .LBB0_509
	s_add_i32 s4, 0, 0x27fc0
	s_waitcnt vmcnt(37)
	v_mov_b32_e32 v0, s4
	s_waitcnt vmcnt(0) expcnt(0) lgkmcnt(0)
	ds_read_b32 v2, v0
	s_add_i32 s4, 0, 0x27fc4
	v_mov_b32_e32 v0, s4
	ds_read_b32 v0, v0
	s_waitcnt lgkmcnt(1)
	v_cmp_ne_u32_e32 vcc, 0, v2
	s_cbranch_vccz .Lcensus_3

.Lcensus_3:
	v_readlane_b32 s4, v253, 8
	s_mul_i32 s31, s77, s4
	s_add_u32 s4, s88, 0x80200
	s_addc_u32 s5, s89, 0
	s_add_u32 s6, s88, 0x80400
	s_addc_u32 s7, s89, 0
	s_add_u32 s8, s88, 0x80500
	s_addc_u32 s9, s89, 0
	s_add_u32 s10, s88, 0x80600
	s_addc_u32 s11, s89, 0
	s_add_u32 s12, s88, 0x80700
	s_addc_u32 s13, s89, 0
	s_add_u32 s14, s88, 0x80800
	s_addc_u32 s15, s89, 0
	s_add_u32 s16, s88, 0x80900
	s_addc_u32 s17, s89, 0
	s_add_u32 s18, s88, 0x80a00
	s_addc_u32 s19, s89, 0
	s_add_u32 s20, s88, 0x80b00
	s_addc_u32 s21, s89, 0
	s_add_u32 s22, s88, 0x80c00
	s_addc_u32 s23, s89, 0
	s_add_u32 s24, s88, 0x80d00
	s_addc_u32 s25, s89, 0
	s_add_u32 s26, s88, 0x80e00
	s_addc_u32 s27, s89, 0
	s_add_u32 s28, s88, 0x80f00
	s_addc_u32 s29, s89, 0
	s_add_u32 s34, s88, 0x81000
	s_addc_u32 s35, s89, 0
	s_add_u32 s36, s88, 0x81100
	s_addc_u32 s37, s89, 0
	s_add_u32 s38, s88, 0x81200
	s_addc_u32 s39, s89, 0
	s_add_u32 s48, s88, 0x81300
	s_mul_i32 s31, s31, s76
	s_addc_u32 s49, s89, 0
	s_mov_b32 s33, 1
	v_mov_b32_e32 v16, 0
	s_branch .LBB0_461

.Lcensus_5:
	v_readlane_b32 s4, v253, 8
	s_mul_i32 s31, s77, s4
	s_add_u32 s4, s88, 0x80200
	s_addc_u32 s5, s89, 0
	s_add_u32 s6, s88, 0x80400
	s_addc_u32 s7, s89, 0
	s_add_u32 s8, s88, 0x80500
	s_addc_u32 s9, s89, 0
	s_add_u32 s12, s88, 0x80600
	s_addc_u32 s13, s89, 0
	s_add_u32 s14, s88, 0x80700
	s_addc_u32 s15, s89, 0
	s_add_u32 s16, s88, 0x80800
	s_addc_u32 s17, s89, 0
	s_add_u32 s18, s88, 0x80900
	s_addc_u32 s19, s89, 0
	s_add_u32 s20, s88, 0x80a00
	s_addc_u32 s21, s89, 0
	s_add_u32 s22, s88, 0x80b00
	s_addc_u32 s23, s89, 0
	s_add_u32 s24, s88, 0x80c00
	s_addc_u32 s25, s89, 0
	s_add_u32 s26, s88, 0x80d00
	s_addc_u32 s27, s89, 0
	s_add_u32 s28, s88, 0x80e00
	s_addc_u32 s29, s89, 0
	s_add_u32 s34, s88, 0x80f00
	s_addc_u32 s35, s89, 0
	s_add_u32 s36, s88, 0x81000
	s_addc_u32 s37, s89, 0
	s_add_u32 s38, s88, 0x81100
	s_addc_u32 s39, s89, 0
	s_add_u32 s44, s88, 0x81200
	s_addc_u32 s45, s89, 0
	s_add_u32 s48, s88, 0x81300
	s_mul_i32 s31, s31, s76
	s_addc_u32 s49, s89, 0
	s_mov_b32 s33, 1
	v_mov_b32_e32 v16, 0
	s_branch .LBB0_603

.Lcensus_6:
	v_readlane_b32 s4, v253, 8
	s_mul_i32 s31, s77, s4
	s_add_u32 s4, s88, 0x80200
	s_addc_u32 s5, s89, 0
	s_add_u32 s6, s88, 0x80400
	s_addc_u32 s7, s89, 0
	s_add_u32 s8, s88, 0x80500
	s_addc_u32 s9, s89, 0
	s_add_u32 s10, s88, 0x80600
	s_addc_u32 s11, s89, 0
	s_add_u32 s14, s88, 0x80700
	s_addc_u32 s15, s89, 0
	s_add_u32 s16, s88, 0x80800
	s_addc_u32 s17, s89, 0
	s_add_u32 s18, s88, 0x80900
	s_addc_u32 s19, s89, 0
	s_add_u32 s20, s88, 0x80a00
	s_addc_u32 s21, s89, 0
	s_add_u32 s22, s88, 0x80b00
	s_addc_u32 s23, s89, 0
	s_add_u32 s24, s88, 0x80c00
	s_addc_u32 s25, s89, 0
	s_add_u32 s26, s88, 0x80d00
	s_addc_u32 s27, s89, 0
	s_add_u32 s28, s88, 0x80e00
	s_addc_u32 s29, s89, 0
	s_add_u32 s34, s88, 0x80f00
	s_addc_u32 s35, s89, 0
	s_add_u32 s36, s88, 0x81000
	s_addc_u32 s37, s89, 0
	s_add_u32 s38, s88, 0x81100
	s_addc_u32 s39, s89, 0
	s_add_u32 s42, s88, 0x81200
	s_addc_u32 s43, s89, 0
	s_add_u32 s44, s88, 0x81300
	s_mul_i32 s31, s31, s76
	s_addc_u32 s45, s89, 0
	s_mov_b32 s33, 1
	v_mov_b32_e32 v16, 0
	s_branch .LBB0_668

.Lcensus_7:
	v_readlane_b32 s4, v253, 8
	s_mul_i32 s31, s77, s4
	s_add_u32 s4, s88, 0x80200
	s_addc_u32 s5, s89, 0
	s_add_u32 s8, s88, 0x80400
	s_addc_u32 s9, s89, 0
	s_add_u32 s10, s88, 0x80500
	s_addc_u32 s11, s89, 0
	s_add_u32 s12, s88, 0x80600
	s_addc_u32 s13, s89, 0
	s_add_u32 s14, s88, 0x80700
	s_addc_u32 s15, s89, 0
	s_add_u32 s16, s88, 0x80800
	s_addc_u32 s17, s89, 0
	s_add_u32 s18, s88, 0x80900
	s_addc_u32 s19, s89, 0
	s_add_u32 s20, s88, 0x80a00
	s_addc_u32 s21, s89, 0
	s_add_u32 s22, s88, 0x80b00
	s_addc_u32 s23, s89, 0
	s_add_u32 s24, s88, 0x80c00
	s_addc_u32 s25, s89, 0
	s_add_u32 s26, s88, 0x80d00
	s_addc_u32 s27, s89, 0
	s_add_u32 s28, s88, 0x80e00
	s_addc_u32 s29, s89, 0
	s_add_u32 s34, s88, 0x80f00
	s_addc_u32 s35, s89, 0
	s_add_u32 s36, s88, 0x81000
	s_addc_u32 s37, s89, 0
	s_add_u32 s38, s88, 0x81100
	s_addc_u32 s39, s89, 0
	s_add_u32 s42, s88, 0x81200
	s_addc_u32 s43, s89, 0
	s_add_u32 s44, s88, 0x81300
	s_mul_i32 s31, s31, s76
	s_addc_u32 s45, s89, 0
	s_mov_b32 s33, 1
	v_mov_b32_e32 v16, 0
	s_branch .LBB0_748

.Lcensus_9:
	v_readlane_b32 s4, v253, 8
	s_mul_i32 s31, s77, s4
	s_add_u32 s4, s88, 0x80200
	s_addc_u32 s5, s89, 0
	s_add_u32 s6, s88, 0x80400
	s_addc_u32 s7, s89, 0
	s_add_u32 s8, s88, 0x80500
	s_addc_u32 s9, s89, 0
	s_add_u32 s10, s88, 0x80600
	s_addc_u32 s11, s89, 0
	s_add_u32 s12, s88, 0x80700
	s_addc_u32 s13, s89, 0
	s_add_u32 s14, s88, 0x80800
	s_addc_u32 s15, s89, 0
	s_add_u32 s16, s88, 0x80900
	s_addc_u32 s17, s89, 0
	s_add_u32 s18, s88, 0x80a00
	s_addc_u32 s19, s89, 0
	s_add_u32 s20, s88, 0x80b00
	s_addc_u32 s21, s89, 0
	s_add_u32 s22, s88, 0x80c00
	s_addc_u32 s23, s89, 0
	s_add_u32 s24, s88, 0x80d00
	s_addc_u32 s25, s89, 0
	s_add_u32 s26, s88, 0x80e00
	s_addc_u32 s27, s89, 0
	s_add_u32 s28, s88, 0x80f00
	s_addc_u32 s29, s89, 0
	s_add_u32 s34, s88, 0x81000
	s_addc_u32 s35, s89, 0
	s_add_u32 s36, s88, 0x81100
	s_addc_u32 s37, s89, 0
	s_add_u32 s38, s88, 0x81200
	s_addc_u32 s39, s89, 0
	s_add_u32 s42, s88, 0x81300
	s_mul_i32 s31, s31, s76
	s_addc_u32 s43, s89, 0
	s_mov_b32 s33, 1
	v_mov_b32_e32 v16, 0
	s_branch .LBB0_964

.Lcensus_11:
	v_readlane_b32 s6, v253, 8
	s_mul_i32 s31, s77, s6
	s_add_u32 s6, s88, 0x80200
	s_addc_u32 s7, s89, 0
	s_add_u32 s8, s88, 0x80400
	s_addc_u32 s9, s89, 0
	s_add_u32 s10, s88, 0x80500
	s_addc_u32 s11, s89, 0
	s_add_u32 s12, s88, 0x80600
	s_addc_u32 s13, s89, 0
	s_add_u32 s14, s88, 0x80700
	s_addc_u32 s15, s89, 0
	s_add_u32 s16, s88, 0x80800
	s_addc_u32 s17, s89, 0
	s_add_u32 s18, s88, 0x80900
	s_addc_u32 s19, s89, 0
	s_add_u32 s20, s88, 0x80a00
	s_addc_u32 s21, s89, 0
	s_add_u32 s22, s88, 0x80b00
	s_addc_u32 s23, s89, 0
	s_add_u32 s24, s88, 0x80c00
	s_addc_u32 s25, s89, 0
	s_add_u32 s26, s88, 0x80d00
	s_addc_u32 s27, s89, 0
	s_add_u32 s28, s88, 0x80e00
	s_addc_u32 s29, s89, 0
	s_add_u32 s34, s88, 0x80f00
	s_addc_u32 s35, s89, 0
	s_add_u32 s36, s88, 0x81000
	s_addc_u32 s37, s89, 0
	s_add_u32 s38, s88, 0x81100
	s_addc_u32 s39, s89, 0
	s_add_u32 s42, s88, 0x81200
	s_addc_u32 s43, s89, 0
	s_add_u32 s44, s88, 0x81300
	s_mul_i32 s31, s31, s76
	s_addc_u32 s45, s89, 0
	s_mov_b32 s33, 1
	v_mov_b32_e32 v16, 0
	s_branch .LBB0_1117
